# grid barrier: release counter replicated per XCD (each leader adds to all replicas, pollers watch their own XCD's word) so 32 instead of 255 pollers share a line
# speedup vs baseline: 1.0049x; 1.0049x over previous
; __device__ __forceinline__ unsigned xb_ld(unsigned* p)              { return __hip_atomic_load(p, __ATOMIC_RELAXED, __HIP_MEMORY_SCOPE_AGENT); }
; __device__ __forceinline__ unsigned xb_add(unsigned* p, unsigned v) { return __hip_atomic_fetch_add(p, v, __ATOMIC_RELAXED, __HIP_MEMORY_SCOPE_AGENT); }
; #define XB_SPIN(cond, bar) do { unsigned _sp = 0; while (cond) { __builtin_amdgcn_s_sleep(1); \
;     if ((++_sp & 255u) == 0u) { if (xb_ld(&(bar)[XB_TMO])) break; if (_sp > XB_SPIN_CAP) { atomicAdd(&(bar)[XB_TMO], 1u); break; } } } } while (0)
; __device__ __forceinline__ void xcd_barrier(const XcdBarrier& b, const int wv) {
;     ...
;         const unsigned old = xb_add(&bar[XB_XSUB(bx)], 1u);
;         const unsigned gen = old / nloc;
;         if (old + 1u == (gen + 1u) * nloc) {
;             __builtin_amdgcn_fence(__ATOMIC_RELEASE, "agent");
;             asm volatile("s_waitcnt vmcnt(0)" ::: "memory");
;             const unsigned og = xb_add(&bar[XB_TOP], 1u);
;             const unsigned tg = og / nx;
;             __builtin_amdgcn_fence(__ATOMIC_ACQUIRE, "agent");
;             if (og + 1u == (tg + 1u) * nx) xb_add(&bar[XB_TOPGEN], 1u);
;             else XB_SPIN(xb_ld(&bar[XB_TOPGEN]) == tg, bar);
;             asm volatile("s_waitcnt vmcnt(0)" ::: "memory");
;         } else {
;             __builtin_amdgcn_fence(__ATOMIC_ACQUIRE, "agent");
;             XB_SPIN(xb_ld(&bar[XB_TOPGEN]) == gen, bar);
.LBB0_171:
	s_or_b64 exec, exec, s[8:9]
	v_cvt_f32_u32_e32 v5, v3
	s_waitcnt vmcnt(0)
	v_readfirstlane_b32 s6, v4
	v_sub_u32_e32 v4, 0, v3
	v_rcp_iflag_f32_e32 v5, v5
	v_add_u32_e32 v6, s6, v2
	v_mul_f32_e32 v5, 0x4f7ffffe, v5
	v_cvt_u32_f32_e32 v5, v5
	v_mul_lo_u32 v2, v4, v5
	v_mul_hi_u32 v2, v5, v2
	v_add_u32_e32 v2, v5, v2
	v_mul_hi_u32 v2, v6, v2
	v_mul_lo_u32 v4, v2, v3
	v_sub_u32_e32 v4, v6, v4
	v_add_u32_e32 v5, 1, v2
	v_cmp_ge_u32_e32 vcc, v4, v3
	s_nop 1
	v_cndmask_b32_e32 v2, v2, v5, vcc
	v_sub_u32_e32 v5, v4, v3
	v_cndmask_b32_e32 v4, v4, v5, vcc
	v_add_u32_e32 v5, 1, v2
	v_cmp_ge_u32_e32 vcc, v4, v3
	v_add_u32_e32 v4, 1, v6
	s_nop 0
	v_cndmask_b32_e32 v2, v2, v5, vcc
	v_mul_lo_u32 v5, v3, v2
	v_add_u32_e32 v3, v5, v3
	v_cmp_ne_u32_e32 vcc, v4, v3
	s_and_saveexec_b64 s[6:7], vcc
	s_xor_b64 s[6:7], exec, s[6:7]
	s_cbranch_execz .LBB0_185
	s_waitcnt lgkmcnt(0)
	v_add_u32_e32 v4, 1, v2
	v_mul_lo_u32 v4, v4, v1
	s_lshl_b32 s10, s20, 8
	s_addk_i32 s10, 0x2400
	s_add_u32 s10, s4, s10
	s_addc_u32 s11, s5, 0
	buffer_inv sc1
	v_mov_b32_e32 v1, 0
	global_load_dword v1, v1, s[10:11] sc1
	s_waitcnt vmcnt(0)
	v_cmp_lt_u32_e32 vcc, v1, v4
	s_and_saveexec_b64 s[8:9], vcc
	s_cbranch_execz .LBB0_184
	s_mov_b32 s22, 1
	s_mov_b64 s[12:13], 0
	v_mov_b32_e32 v1, 0
	s_branch .LBB0_175

; __device__ __forceinline__ unsigned xb_ld(unsigned* p)              { return __hip_atomic_load(p, __ATOMIC_RELAXED, __HIP_MEMORY_SCOPE_AGENT); }
; __device__ __forceinline__ unsigned xb_add(unsigned* p, unsigned v) { return __hip_atomic_fetch_add(p, v, __ATOMIC_RELAXED, __HIP_MEMORY_SCOPE_AGENT); }
; #define XB_SPIN(cond, bar) do { unsigned _sp = 0; while (cond) { __builtin_amdgcn_s_sleep(1); \
;     if ((++_sp & 255u) == 0u) { if (xb_ld(&(bar)[XB_TMO])) break; if (_sp > XB_SPIN_CAP) { atomicAdd(&(bar)[XB_TMO], 1u); break; } } } } while (0)
; __device__ __forceinline__ void xcd_barrier(const XcdBarrier& b, const int wv) {
;     ...
;         const unsigned old = xb_add(&bar[XB_XSUB(bx)], 1u);
;         const unsigned gen = old / nloc;
;         if (old + 1u == (gen + 1u) * nloc) {
;             __builtin_amdgcn_fence(__ATOMIC_RELEASE, "agent");
;             asm volatile("s_waitcnt vmcnt(0)" ::: "memory");
;             const unsigned og = xb_add(&bar[XB_TOP], 1u);
;             const unsigned tg = og / nx;
;             __builtin_amdgcn_fence(__ATOMIC_ACQUIRE, "agent");
;             if (og + 1u == (tg + 1u) * nx) xb_add(&bar[XB_TOPGEN], 1u);
;             else XB_SPIN(xb_ld(&bar[XB_TOPGEN]) == tg, bar);
;             asm volatile("s_waitcnt vmcnt(0)" ::: "memory");
;         } else {
;             __builtin_amdgcn_fence(__ATOMIC_ACQUIRE, "agent");
;             XB_SPIN(xb_ld(&bar[XB_TOPGEN]) == gen, bar);
;             asm volatile("s_waitcnt vmcnt(0)" ::: "memory");
;         }
.LBB0_185:
	s_andn2_saveexec_b64 s[6:7], s[6:7]
	s_cbranch_execz .LBB0_205
	s_mov_b64 s[6:7], exec
	buffer_wbl2 sc1
	s_waitcnt vmcnt(0) lgkmcnt(0)
	s_waitcnt vmcnt(0)
	v_mbcnt_lo_u32_b32 v2, s6, 0
	v_mbcnt_hi_u32_b32 v2, s7, v2
	v_cmp_eq_u32_e32 vcc, 0, v2
	s_and_saveexec_b64 s[8:9], vcc
	s_cbranch_execz .LBB0_188
	s_add_u32 s12, s4, 0x2400
	s_addc_u32 s13, s5, 0
	v_mov_b32_e32 v5, 0
	v_mov_b32_e32 v6, 1
	global_atomic_add v5, v6, s[12:13]
	global_atomic_add v5, v6, s[12:13] offset:256
	global_atomic_add v5, v6, s[12:13] offset:512
	global_atomic_add v5, v6, s[12:13] offset:768
	global_atomic_add v5, v6, s[12:13] offset:1024
	global_atomic_add v5, v6, s[12:13] offset:1280
	global_atomic_add v5, v6, s[12:13] offset:1536
	global_atomic_add v5, v6, s[12:13] offset:1792
	global_atomic_add v5, v6, s[12:13] offset:2048
	global_atomic_add v5, v6, s[12:13] offset:2304
	global_atomic_add v5, v6, s[12:13] offset:2560
	global_atomic_add v5, v6, s[12:13] offset:2816
	global_atomic_add v5, v6, s[12:13] offset:3072
	global_atomic_add v5, v6, s[12:13] offset:3328
	global_atomic_add v5, v6, s[12:13] offset:3584
	global_atomic_add v5, v6, s[12:13] offset:3840
	s_bcnt1_i32_b64 s6, s[6:7]
	v_mov_b32_e32 v3, 0x3000
	v_mov_b32_e32 v4, s6
	global_atomic_add v3, v3, v4, s[4:5] offset:1024 sc0
.LBB0_188:
	s_or_b64 exec, exec, s[8:9]
	v_cvt_f32_u32_e32 v4, v1
	s_waitcnt vmcnt(0)
	v_readfirstlane_b32 s6, v3
	s_lshl_b32 s8, s20, 8
	s_addk_i32 s8, 0x2400
	s_add_u32 s8, s4, s8
	s_addc_u32 s9, s5, 0
	v_rcp_iflag_f32_e32 v4, v4
	v_add_u32_e32 v2, s6, v2
	s_mov_b64 s[10:11], 0
	buffer_inv sc1
	v_mul_f32_e32 v3, 0x4f7ffffe, v4
	v_cvt_u32_f32_e32 v3, v3
	v_sub_u32_e32 v4, 0, v1
	v_mul_lo_u32 v4, v4, v3
	v_mul_hi_u32 v4, v3, v4
	v_add_u32_e32 v3, v3, v4
	v_mul_hi_u32 v3, v2, v3
	v_mul_lo_u32 v4, v3, v1
	v_sub_u32_e32 v4, v2, v4
	v_add_u32_e32 v5, 1, v3
	v_cmp_ge_u32_e32 vcc, v4, v1
	v_add_u32_e32 v2, 1, v2
	s_nop 0
	v_cndmask_b32_e32 v3, v3, v5, vcc
	v_sub_u32_e32 v5, v4, v1
	v_cndmask_b32_e32 v4, v4, v5, vcc
	v_add_u32_e32 v5, 1, v3
	v_cmp_ge_u32_e32 vcc, v4, v1
	s_nop 1
	v_cndmask_b32_e32 v4, v3, v5, vcc
	v_mul_lo_u32 v3, v1, v4
	v_add_u32_e32 v1, v3, v1
	v_cmp_ne_u32_e32 vcc, v2, v1
	v_mov_b32_e32 v5, v1
	v_mov_b64_e32 v[2:3], s[8:9]
	s_and_saveexec_b64 s[6:7], vcc
	s_cbranch_execz .LBB0_202
	v_mov_b32_e32 v1, 0
	global_load_dword v2, v1, s[8:9] sc1
	s_mov_b64 s[14:15], 0
	s_waitcnt vmcnt(0)
	v_cmp_lt_u32_e32 vcc, v2, v5
	s_and_saveexec_b64 s[12:13], vcc
	s_cbranch_execz .LBB0_201
	s_add_u32 s10, s4, 0x200
	s_addc_u32 s11, s5, 0
	s_mov_b32 s22, 1
	s_mov_b64 s[4:5], 0
	s_branch .LBB0_192

; __device__ __forceinline__ unsigned xb_ld(unsigned* p)              { return __hip_atomic_load(p, __ATOMIC_RELAXED, __HIP_MEMORY_SCOPE_AGENT); }
; __device__ __forceinline__ unsigned xb_add(unsigned* p, unsigned v) { return __hip_atomic_fetch_add(p, v, __ATOMIC_RELAXED, __HIP_MEMORY_SCOPE_AGENT); }
; #define XB_SPIN(cond, bar) do { unsigned _sp = 0; while (cond) { __builtin_amdgcn_s_sleep(1); \
;     if ((++_sp & 255u) == 0u) { if (xb_ld(&(bar)[XB_TMO])) break; if (_sp > XB_SPIN_CAP) { atomicAdd(&(bar)[XB_TMO], 1u); break; } } } } while (0)
; __device__ __forceinline__ void xcd_barrier(const XcdBarrier& b, const int wv) {
;     ...
;         const unsigned old = xb_add(&bar[XB_XSUB(bx)], 1u);
;         const unsigned gen = old / nloc;
;         if (old + 1u == (gen + 1u) * nloc) {
;             __builtin_amdgcn_fence(__ATOMIC_RELEASE, "agent");
;             asm volatile("s_waitcnt vmcnt(0)" ::: "memory");
;             const unsigned og = xb_add(&bar[XB_TOP], 1u);
;             const unsigned tg = og / nx;
;             __builtin_amdgcn_fence(__ATOMIC_ACQUIRE, "agent");
;             if (og + 1u == (tg + 1u) * nx) xb_add(&bar[XB_TOPGEN], 1u);
;             else XB_SPIN(xb_ld(&bar[XB_TOPGEN]) == tg, bar);
;             asm volatile("s_waitcnt vmcnt(0)" ::: "memory");
;         } else {
;             __builtin_amdgcn_fence(__ATOMIC_ACQUIRE, "agent");
;             XB_SPIN(xb_ld(&bar[XB_TOPGEN]) == gen, bar);
.LBB0_370:
	s_or_b64 exec, exec, s[4:5]
	v_cvt_f32_u32_e32 v4, v2
	s_waitcnt vmcnt(0)
	v_readfirstlane_b32 s4, v3
	v_sub_u32_e32 v3, 0, v2
	v_rcp_iflag_f32_e32 v4, v4
	v_add_u32_e32 v5, s4, v1
	v_mul_f32_e32 v4, 0x4f7ffffe, v4
	v_cvt_u32_f32_e32 v4, v4
	v_mul_lo_u32 v1, v3, v4
	v_mul_hi_u32 v1, v4, v1
	v_add_u32_e32 v1, v4, v1
	v_mul_hi_u32 v1, v5, v1
	v_mul_lo_u32 v3, v1, v2
	v_sub_u32_e32 v3, v5, v3
	v_add_u32_e32 v4, 1, v1
	v_cmp_ge_u32_e32 vcc, v3, v2
	s_nop 1
	v_cndmask_b32_e32 v1, v1, v4, vcc
	v_sub_u32_e32 v4, v3, v2
	v_cndmask_b32_e32 v3, v3, v4, vcc
	v_add_u32_e32 v4, 1, v1
	v_cmp_ge_u32_e32 vcc, v3, v2
	v_add_u32_e32 v3, 1, v5
	s_nop 0
	v_cndmask_b32_e32 v1, v1, v4, vcc
	v_mul_lo_u32 v4, v2, v1
	v_add_u32_e32 v2, v4, v2
	v_cmp_ne_u32_e32 vcc, v3, v2
	s_and_saveexec_b64 s[4:5], vcc
	s_xor_b64 s[4:5], exec, s[4:5]
	s_cbranch_execz .LBB0_384
	s_waitcnt lgkmcnt(0)
	v_add_u32_e32 v2, 1, v1
	v_mul_lo_u32 v2, v2, v0
	s_lshl_b32 s8, s18, 8
	s_addk_i32 s8, 0x2400
	s_add_u32 s8, s2, s8
	s_addc_u32 s9, s3, 0
	buffer_inv sc1
	global_load_dword v0, v65, s[8:9] sc1
	s_waitcnt vmcnt(0)
	v_cmp_lt_u32_e32 vcc, v0, v2
	s_and_saveexec_b64 s[6:7], vcc
	s_cbranch_execz .LBB0_383
	s_mov_b32 s20, 1
	s_mov_b64 s[10:11], 0
	s_branch .LBB0_374

; __device__ __forceinline__ unsigned xb_ld(unsigned* p)              { return __hip_atomic_load(p, __ATOMIC_RELAXED, __HIP_MEMORY_SCOPE_AGENT); }
; __device__ __forceinline__ unsigned xb_add(unsigned* p, unsigned v) { return __hip_atomic_fetch_add(p, v, __ATOMIC_RELAXED, __HIP_MEMORY_SCOPE_AGENT); }
; #define XB_SPIN(cond, bar) do { unsigned _sp = 0; while (cond) { __builtin_amdgcn_s_sleep(1); \
;     if ((++_sp & 255u) == 0u) { if (xb_ld(&(bar)[XB_TMO])) break; if (_sp > XB_SPIN_CAP) { atomicAdd(&(bar)[XB_TMO], 1u); break; } } } } while (0)
; __device__ __forceinline__ void xcd_barrier(const XcdBarrier& b, const int wv) {
;     ...
;         const unsigned old = xb_add(&bar[XB_XSUB(bx)], 1u);
;         const unsigned gen = old / nloc;
;         if (old + 1u == (gen + 1u) * nloc) {
;             __builtin_amdgcn_fence(__ATOMIC_RELEASE, "agent");
;             asm volatile("s_waitcnt vmcnt(0)" ::: "memory");
;             const unsigned og = xb_add(&bar[XB_TOP], 1u);
;             const unsigned tg = og / nx;
;             __builtin_amdgcn_fence(__ATOMIC_ACQUIRE, "agent");
;             if (og + 1u == (tg + 1u) * nx) xb_add(&bar[XB_TOPGEN], 1u);
;             else XB_SPIN(xb_ld(&bar[XB_TOPGEN]) == tg, bar);
;             asm volatile("s_waitcnt vmcnt(0)" ::: "memory");
;         } else {
;             __builtin_amdgcn_fence(__ATOMIC_ACQUIRE, "agent");
;             XB_SPIN(xb_ld(&bar[XB_TOPGEN]) == gen, bar);
;             asm volatile("s_waitcnt vmcnt(0)" ::: "memory");
;         }
.LBB0_384:
	s_andn2_saveexec_b64 s[4:5], s[4:5]
	s_cbranch_execz .LBB0_402
	s_mov_b64 s[4:5], exec
	buffer_wbl2 sc1
	s_waitcnt vmcnt(0) lgkmcnt(0)
	s_waitcnt vmcnt(0)
	v_mbcnt_lo_u32_b32 v1, s4, 0
	v_mbcnt_hi_u32_b32 v1, s5, v1
	v_cmp_eq_u32_e32 vcc, 0, v1
	s_and_saveexec_b64 s[6:7], vcc
	s_cbranch_execz .LBB0_387
	s_add_u32 s10, s2, 0x2400
	s_addc_u32 s11, s3, 0
	global_atomic_add v65, v227, s[10:11]
	global_atomic_add v65, v227, s[10:11] offset:256
	global_atomic_add v65, v227, s[10:11] offset:512
	global_atomic_add v65, v227, s[10:11] offset:768
	global_atomic_add v65, v227, s[10:11] offset:1024
	global_atomic_add v65, v227, s[10:11] offset:1280
	global_atomic_add v65, v227, s[10:11] offset:1536
	global_atomic_add v65, v227, s[10:11] offset:1792
	global_atomic_add v65, v227, s[10:11] offset:2048
	global_atomic_add v65, v227, s[10:11] offset:2304
	global_atomic_add v65, v227, s[10:11] offset:2560
	global_atomic_add v65, v227, s[10:11] offset:2816
	global_atomic_add v65, v227, s[10:11] offset:3072
	global_atomic_add v65, v227, s[10:11] offset:3328
	global_atomic_add v65, v227, s[10:11] offset:3584
	global_atomic_add v65, v227, s[10:11] offset:3840
	s_bcnt1_i32_b64 s4, s[4:5]
	v_mov_b32_e32 v2, s4
	v_mov_b32_e32 v3, 0x3000
	global_atomic_add v2, v3, v2, s[2:3] offset:1024 sc0
.LBB0_387:
	s_or_b64 exec, exec, s[6:7]
	v_cvt_f32_u32_e32 v3, v0
	s_waitcnt vmcnt(0)
	v_readfirstlane_b32 s4, v2
	s_lshl_b32 s6, s18, 8
	s_addk_i32 s6, 0x2400
	s_add_u32 s6, s2, s6
	s_addc_u32 s7, s3, 0
	v_rcp_iflag_f32_e32 v3, v3
	v_add_u32_e32 v1, s4, v1
	s_mov_b64 s[8:9], 0
	buffer_inv sc1
	v_mul_f32_e32 v2, 0x4f7ffffe, v3
	v_cvt_u32_f32_e32 v2, v2
	v_sub_u32_e32 v3, 0, v0
	v_mul_lo_u32 v3, v3, v2
	v_mul_hi_u32 v3, v2, v3
	v_add_u32_e32 v2, v2, v3
	v_mul_hi_u32 v2, v1, v2
	v_mul_lo_u32 v3, v2, v0
	v_sub_u32_e32 v3, v1, v3
	v_add_u32_e32 v4, 1, v2
	v_cmp_ge_u32_e32 vcc, v3, v0
	v_add_u32_e32 v1, 1, v1
	s_nop 0
	v_cndmask_b32_e32 v2, v2, v4, vcc
	v_sub_u32_e32 v4, v3, v0
	v_cndmask_b32_e32 v3, v3, v4, vcc
	v_add_u32_e32 v4, 1, v2
	v_cmp_ge_u32_e32 vcc, v3, v0
	s_nop 1
	v_cndmask_b32_e32 v2, v2, v4, vcc
	v_mul_lo_u32 v3, v0, v2
	v_add_u32_e32 v0, v3, v0
	v_cmp_ne_u32_e32 vcc, v1, v0
	v_mov_b32_e32 v3, v0
	v_mov_b64_e32 v[0:1], s[6:7]
	s_and_saveexec_b64 s[4:5], vcc
	s_cbranch_execz .LBB0_399
	global_load_dword v0, v65, s[6:7] sc1
	s_mov_b64 s[12:13], 0
	s_waitcnt vmcnt(0)
	v_cmp_lt_u32_e32 vcc, v0, v3
	s_and_saveexec_b64 s[10:11], vcc
	s_cbranch_execz .LBB0_398
	s_add_u32 s8, s2, 0x200
	s_addc_u32 s9, s3, 0
	s_mov_b32 s20, 1
	s_mov_b64 s[2:3], 0
	s_branch .LBB0_391
